# plain stores everywhere; cvt3: every 64th block issues buffer_wbl2 so the L2 write-back happens during the kernel instead of at its end
# baseline (speedup 1.0000x reference)
.LBB0_9:
	s_ashr_i32 s9, s8, 31
	s_lshl_b64 s[10:11], s[8:9], 14
	s_waitcnt lgkmcnt(0)
	s_add_u32 s4, s4, s10
	s_addc_u32 s5, s5, s11
	v_lshlrev_b32_e32 v18, 4, v0
	v_mov_b32_e32 v19, 0
	v_lshl_add_u64 v[14:15], s[4:5], 0, v[18:19]
	s_movk_i32 s3, 0x2000
	v_add_co_u32_e32 v16, vcc, s3, v14
	s_movk_i32 s3, 0x3000
	s_nop 0
	v_addc_co_u32_e32 v17, vcc, 0, v15, vcc
	global_load_dwordx4 v[2:5], v18, s[4:5] nt
	v_add_co_u32_e32 v14, vcc, s3, v14
	global_load_dwordx4 v[6:9], v[16:17], off offset:-4096 nt
	global_load_dwordx4 v[10:13], v[16:17], off nt
	v_addc_co_u32_e32 v15, vcc, 0, v15, vcc
	global_load_dwordx4 v[14:17], v[14:15], off nt
	s_lshl_b64 s[4:5], s[8:9], 13
	s_add_u32 s4, s6, s4
	s_addc_u32 s5, s7, s5
	v_lshlrev_b32_e32 v18, 3, v0
	v_lshl_add_u64 v[20:21], s[4:5], 0, v[18:19]
	v_add_co_u32_e32 v20, vcc, 0x1000, v20
	s_waitcnt vmcnt(3)
	v_cvt_pk_f16_f32 v2, v2, v3
	v_cvt_pk_f16_f32 v3, v4, v5
	global_store_dwordx2 v18, v[2:3], s[4:5]
	s_waitcnt vmcnt(3)
	v_cvt_pk_f16_f32 v2, v6, v7
	v_cvt_pk_f16_f32 v3, v8, v9
	v_addc_co_u32_e32 v21, vcc, 0, v21, vcc
	s_waitcnt vmcnt(2)
	v_cvt_pk_f16_f32 v4, v10, v11
	v_cvt_pk_f16_f32 v5, v12, v13
	s_waitcnt vmcnt(1)
	v_cvt_pk_f16_f32 v6, v14, v15
	v_cvt_pk_f16_f32 v7, v16, v17
	global_store_dwordx2 v18, v[2:3], s[4:5] offset:2048
	global_store_dwordx2 v[20:21], v[4:5], off
	global_store_dwordx2 v[20:21], v[6:7], off offset:2048
	s_and_b32 s3, s8, 63
	s_cmp_lg_u32 s3, 63
	s_cbranch_scc1 .Lcvt_nowb
	buffer_wbl2 sc1
.Lcvt_nowb:
	s_mov_b64 s[4:5], 0
